# stack + gate/up L1 row-map wait deferred (same as L0)
# speedup vs baseline: 1.0088x; 1.0031x over previous
.LBB0_3342:
	s_nop 0
	v_cndmask_b32_e64 v2, 0, 1, s[10:11]
	v_cmp_ne_u32_e64 s[8:9], 1, v2
	s_andn2_b64 vcc, exec, s[10:11]
	v_mov_b32_e32 v148, v150
	v_mov_b32_e32 v146, v152
	v_mov_b32_e32 v173, v154
	v_mov_b32_e32 v172, v142
	s_cbranch_vccnz .LBB0_3344
	s_ashr_i32 s67, s66, 31
	s_lshl_b64 s[72:73], s[66:67], 10
	s_add_u32 s72, s4, s72
	s_addc_u32 s73, s5, s73
	global_load_dword v200, v1, s[72:73]
	global_load_dword v201, v162, s[72:73]
	global_load_dword v252, v162, s[72:73] offset:512
	global_load_dword v253, v1, s[72:73] offset:512
.LBB0_3344:
	ds_read_b128 v[2:5], v167
	ds_read_b128 v[6:9], v167 offset:1024
	ds_read_b128 v[180:183], v167 offset:2048
	ds_read_b128 v[184:187], v167 offset:3072
	ds_read_b128 v[188:191], v168
	ds_read_b128 v[192:195], v168 offset:1024
	ds_read_b128 v[204:207], v168 offset:2048
	ds_read_b128 v[208:211], v168 offset:3072
	s_ashr_i32 s71, s70, 31
	s_ashr_i32 s65, s64, 31
	s_lshl_b64 s[72:73], s[70:71], 21
	s_lshl_b64 s[82:83], s[64:65], 18
	s_add_u32 s65, s1, s72
	s_addc_u32 s67, s3, s73
	s_add_u32 s72, s65, s82
	s_addc_u32 s73, s67, s83
	s_and_b64 s[10:11], s[10:11], exec
	s_cselect_b32 s11, s73, s79
	s_cselect_b32 s10, s72, s78
	ds_read_b128 v[10:13], v166
	ds_read_b128 v[14:17], v166 offset:1024
	ds_read_b128 v[18:21], v166 offset:2048
	ds_read_b128 v[22:25], v166 offset:3072
	ds_read_b128 v[26:29], v166 offset:4096
	ds_read_b128 v[30:33], v166 offset:5120
	ds_read_b128 v[34:37], v166 offset:6144
	ds_read_b128 v[38:41], v166 offset:7168
	s_waitcnt vmcnt(22)
	s_waitcnt lgkmcnt(0)
	s_barrier
	s_setprio 1
	s_waitcnt lgkmcnt(0)
	v_mfma_f32_16x16x128_f8f6f4 v[130:133], v[2:9], v[10:17], 0
	v_mfma_f32_16x16x128_f8f6f4 v[122:125], v[180:187], v[10:17], 0
	v_mfma_f32_16x16x128_f8f6f4 v[114:117], v[2:9], v[18:25], 0
	v_mfma_f32_16x16x128_f8f6f4 v[106:109], v[180:187], v[18:25], 0
	v_mfma_f32_16x16x128_f8f6f4 v[98:101], v[2:9], v[26:33], 0
	v_mfma_f32_16x16x128_f8f6f4 v[90:93], v[180:187], v[26:33], 0
	v_mfma_f32_16x16x128_f8f6f4 v[82:85], v[2:9], v[34:41], 0
	v_mfma_f32_16x16x128_f8f6f4 v[66:69], v[180:187], v[34:41], 0
	s_setprio 0
	s_setprio 1
	v_mfma_f32_16x16x128_f8f6f4 v[134:137], v[188:195], v[10:17], 0
	v_mfma_f32_16x16x128_f8f6f4 v[126:129], v[204:211], v[10:17], 0
	v_mfma_f32_16x16x128_f8f6f4 v[118:121], v[188:195], v[18:25], 0
	v_mfma_f32_16x16x128_f8f6f4 v[110:113], v[204:211], v[18:25], 0
	v_mfma_f32_16x16x128_f8f6f4 v[102:105], v[188:195], v[26:33], 0
	v_mfma_f32_16x16x128_f8f6f4 v[94:97], v[204:211], v[26:33], 0
	v_mfma_f32_16x16x128_f8f6f4 v[86:89], v[188:195], v[34:41], 0
	v_mfma_f32_16x16x128_f8f6f4 v[74:77], v[204:211], v[34:41], 0
	s_setprio 0
	s_barrier
	s_add_i32 s86, s77, s33
	v_lshl_add_u64 v[156:157], s[78:79], 0, v[138:139]
	s_add_i32 s82, s86, 0x2000
	v_lshl_add_u64 v[10:11], v[156:157], 0, s[42:43]
	s_mov_b32 m0, s86
	v_lshl_add_u64 v[158:159], s[78:79], 0, v[140:141]
	s_add_u32 s84, s78, 0x8100
	ds_read_b128 v[212:215], v166 offset:16384
	ds_read_b128 v[216:219], v166 offset:17408
	ds_read_b128 v[220:223], v166 offset:18432
	ds_read_b128 v[224:227], v166 offset:19456
	ds_read_b128 v[228:231], v166 offset:20480
	ds_read_b128 v[232:235], v166 offset:21504
	ds_read_b128 v[236:239], v166 offset:22528
	ds_read_b128 v[240:243], v166 offset:23552
	global_load_lds_dwordx4 v[10:11], off
	v_lshl_add_u64 v[10:11], v[158:159], 0, s[42:43]
	s_mov_b32 m0, s82
	s_addc_u32 s85, s79, 0
	s_add_i32 s83, s80, s33
	global_load_lds_dwordx4 v[10:11], off
	v_lshl_add_u64 v[10:11], s[84:85], 0, v[138:139]
	s_mov_b32 m0, s83
	s_nop 0
	global_load_lds_dwordx4 v[10:11], off
	v_lshl_add_u64 v[10:11], s[84:85], 0, v[140:141]
	s_add_i32 s84, s83, 0x2000
	s_mov_b32 m0, s84
	s_nop 0
	global_load_lds_dwordx4 v[10:11], off
	s_mov_b32 m0, s55
	s_nop 0
	global_load_lds_dwordx4 v142, s[24:25]
	s_mov_b32 m0, s56
	s_nop 0
	global_load_lds_dwordx4 v154, s[24:25]
	s_waitcnt vmcnt(22)
	s_waitcnt lgkmcnt(0)
	s_barrier
	s_setprio 1
	s_waitcnt lgkmcnt(0)
	v_mfma_f32_16x16x128_f8f6f4 v[70:73], v[2:9], v[212:219], 0
	v_mfma_f32_16x16x128_f8f6f4 v[58:61], v[180:187], v[212:219], 0
	v_mfma_f32_16x16x128_f8f6f4 v[50:53], v[2:9], v[220:227], 0
	v_mfma_f32_16x16x128_f8f6f4 v[34:37], v[180:187], v[220:227], 0
	v_mfma_f32_16x16x128_f8f6f4 v[26:29], v[2:9], v[228:235], 0
	v_mfma_f32_16x16x128_f8f6f4 v[18:21], v[180:187], v[228:235], 0
	v_mfma_f32_16x16x128_f8f6f4 v[10:13], v[2:9], v[236:243], 0
	v_mfma_f32_16x16x128_f8f6f4 v[2:5], v[180:187], v[236:243], 0
	s_setprio 0
	s_setprio 1
	v_mfma_f32_16x16x128_f8f6f4 v[78:81], v[188:195], v[212:219], 0
	v_mfma_f32_16x16x128_f8f6f4 v[62:65], v[204:211], v[212:219], 0
	v_mfma_f32_16x16x128_f8f6f4 v[54:57], v[188:195], v[220:227], 0
	v_mfma_f32_16x16x128_f8f6f4 v[38:41], v[204:211], v[220:227], 0
	v_mfma_f32_16x16x128_f8f6f4 v[30:33], v[188:195], v[228:235], 0
	v_mfma_f32_16x16x128_f8f6f4 v[22:25], v[204:211], v[228:235], 0
	v_mfma_f32_16x16x128_f8f6f4 v[14:17], v[188:195], v[236:243], 0
	v_mfma_f32_16x16x128_f8f6f4 v[6:9], v[204:211], v[236:243], 0
	s_setprio 0
	s_barrier
	s_add_i32 s85, 0, 0x18000
	s_add_i32 s67, 0, 0x1c000
	v_add_u32_e32 v147, s85, v165
	v_add_u32_e32 v149, s67, v165
	ds_read_b128 v[180:183], v147
	ds_read_b128 v[184:187], v147 offset:1024
	ds_read_b128 v[188:191], v147 offset:2048
	ds_read_b128 v[192:195], v147 offset:3072
	ds_read_b128 v[204:207], v149
	ds_read_b128 v[208:211], v149 offset:1024
	ds_read_b128 v[212:215], v149 offset:2048
	ds_read_b128 v[216:219], v149 offset:3072
	s_mov_b32 m0, s57
	ds_read_b128 v[220:223], v166 offset:32768
	ds_read_b128 v[224:227], v166 offset:33792
	ds_read_b128 v[228:231], v166 offset:34816
	ds_read_b128 v[232:235], v166 offset:35840
	ds_read_b128 v[236:239], v166 offset:36864
	ds_read_b128 v[240:243], v166 offset:37888
	ds_read_b128 v[244:247], v166 offset:38912
	ds_read_b128 v[248:251], v166 offset:39936
	global_load_lds_dwordx4 v152, s[24:25]
	s_mov_b32 m0, s58
	s_nop 0
	global_load_lds_dwordx4 v150, s[24:25]
	s_waitcnt vmcnt(22)
	s_waitcnt lgkmcnt(0)
	s_barrier
	s_setprio 1
	s_waitcnt lgkmcnt(0)
	v_mfma_f32_16x16x128_f8f6f4 v[130:133], v[180:187], v[220:227], v[130:133]
	v_mfma_f32_16x16x128_f8f6f4 v[122:125], v[188:195], v[220:227], v[122:125]
	v_mfma_f32_16x16x128_f8f6f4 v[114:117], v[180:187], v[228:235], v[114:117]
	v_mfma_f32_16x16x128_f8f6f4 v[106:109], v[188:195], v[228:235], v[106:109]
	v_mfma_f32_16x16x128_f8f6f4 v[98:101], v[180:187], v[236:243], v[98:101]
	v_mfma_f32_16x16x128_f8f6f4 v[90:93], v[188:195], v[236:243], v[90:93]
	v_mfma_f32_16x16x128_f8f6f4 v[82:85], v[180:187], v[244:251], v[82:85]
	v_mfma_f32_16x16x128_f8f6f4 v[66:69], v[188:195], v[244:251], v[66:69]
	s_setprio 0
	s_setprio 1
	v_mfma_f32_16x16x128_f8f6f4 v[134:137], v[204:211], v[220:227], v[134:137]
	v_mfma_f32_16x16x128_f8f6f4 v[126:129], v[212:219], v[220:227], v[126:129]
	v_mfma_f32_16x16x128_f8f6f4 v[118:121], v[204:211], v[228:235], v[118:121]
	v_mfma_f32_16x16x128_f8f6f4 v[110:113], v[212:219], v[228:235], v[110:113]
	v_mfma_f32_16x16x128_f8f6f4 v[102:105], v[204:211], v[236:243], v[102:105]
	v_mfma_f32_16x16x128_f8f6f4 v[94:97], v[212:219], v[236:243], v[94:97]
	v_mfma_f32_16x16x128_f8f6f4 v[86:89], v[204:211], v[244:251], v[86:89]
	v_mfma_f32_16x16x128_f8f6f4 v[74:77], v[212:219], v[244:251], v[74:77]
	s_setprio 0
	s_barrier
	s_add_i32 s85, s85, s33
	s_add_i32 s65, s85, 0x2000
	v_lshl_add_u64 v[160:161], v[156:157], 0, s[44:45]
	s_mov_b32 m0, s85
	s_add_u32 s88, s78, 0x8180
	ds_read_b128 v[220:223], v166 offset:49152
	ds_read_b128 v[224:227], v166 offset:50176
	ds_read_b128 v[228:231], v166 offset:51200
	ds_read_b128 v[232:235], v166 offset:52224
	ds_read_b128 v[236:239], v166 offset:53248
	ds_read_b128 v[240:243], v166 offset:54272
	ds_read_b128 v[244:247], v166 offset:55296
	ds_read_b128 v[248:251], v166 offset:56320
	global_load_lds_dwordx4 v[160:161], off
	v_lshl_add_u64 v[160:161], v[158:159], 0, s[44:45]
	s_mov_b32 m0, s65
	s_addc_u32 s89, s79, 0
	s_add_i32 s67, s67, s33
	global_load_lds_dwordx4 v[160:161], off
	v_lshl_add_u64 v[160:161], s[88:89], 0, v[138:139]
	s_mov_b32 m0, s67
	s_add_i32 s68, s67, 0x2000
	global_load_lds_dwordx4 v[160:161], off
	v_lshl_add_u64 v[160:161], s[88:89], 0, v[140:141]
	s_mov_b32 m0, s68
	s_nop 0
	global_load_lds_dwordx4 v[160:161], off
	s_mov_b32 m0, s59
	s_nop 0
	global_load_lds_dwordx4 v142, s[26:27]
	s_mov_b32 m0, s60
	s_nop 0
	global_load_lds_dwordx4 v154, s[26:27]
	s_waitcnt vmcnt(8)
	s_waitcnt lgkmcnt(0)
	s_barrier
	s_setprio 1
	s_waitcnt lgkmcnt(0)
	v_mfma_f32_16x16x128_f8f6f4 v[70:73], v[180:187], v[220:227], v[70:73]
	v_mfma_f32_16x16x128_f8f6f4 v[58:61], v[188:195], v[220:227], v[58:61]
	v_mfma_f32_16x16x128_f8f6f4 v[50:53], v[180:187], v[228:235], v[50:53]
	v_mfma_f32_16x16x128_f8f6f4 v[34:37], v[188:195], v[228:235], v[34:37]
	v_mfma_f32_16x16x128_f8f6f4 v[26:29], v[180:187], v[236:243], v[26:29]
	v_mfma_f32_16x16x128_f8f6f4 v[18:21], v[188:195], v[236:243], v[18:21]
	v_mfma_f32_16x16x128_f8f6f4 v[10:13], v[180:187], v[244:251], v[10:13]
	v_mfma_f32_16x16x128_f8f6f4 v[2:5], v[188:195], v[244:251], v[2:5]
	s_setprio 0
	s_setprio 1
	v_mfma_f32_16x16x128_f8f6f4 v[78:81], v[204:211], v[220:227], v[78:81]
	v_mfma_f32_16x16x128_f8f6f4 v[62:65], v[212:219], v[220:227], v[62:65]
	v_mfma_f32_16x16x128_f8f6f4 v[54:57], v[204:211], v[228:235], v[54:57]
	v_mfma_f32_16x16x128_f8f6f4 v[38:41], v[212:219], v[228:235], v[38:41]
	v_mfma_f32_16x16x128_f8f6f4 v[30:33], v[204:211], v[236:243], v[30:33]
	v_mfma_f32_16x16x128_f8f6f4 v[22:25], v[212:219], v[236:243], v[22:25]
	v_mfma_f32_16x16x128_f8f6f4 v[14:17], v[204:211], v[244:251], v[14:17]
	v_mfma_f32_16x16x128_f8f6f4 v[6:9], v[212:219], v[244:251], v[6:9]
	s_setprio 0
	s_barrier
	ds_read_b128 v[180:183], v167
	ds_read_b128 v[184:187], v167 offset:1024
	ds_read_b128 v[188:191], v167 offset:2048
	ds_read_b128 v[192:195], v167 offset:3072
	ds_read_b128 v[204:207], v168
	ds_read_b128 v[208:211], v168 offset:1024
	ds_read_b128 v[212:215], v168 offset:2048
	ds_read_b128 v[216:219], v168 offset:3072
	s_mov_b32 m0, s61
	ds_read_b128 v[220:223], v166
	ds_read_b128 v[224:227], v166 offset:1024
	ds_read_b128 v[228:231], v166 offset:2048
	ds_read_b128 v[232:235], v166 offset:3072
	ds_read_b128 v[236:239], v166 offset:4096
	ds_read_b128 v[240:243], v166 offset:5120
	ds_read_b128 v[244:247], v166 offset:6144
	ds_read_b128 v[248:251], v166 offset:7168
	global_load_lds_dwordx4 v152, s[26:27]
	s_mov_b32 m0, s69
	s_nop 0
	global_load_lds_dwordx4 v150, s[26:27]
	s_waitcnt vmcnt(8)
	s_waitcnt lgkmcnt(0)
	s_barrier
	s_setprio 1
	s_waitcnt lgkmcnt(0)
	v_mfma_f32_16x16x128_f8f6f4 v[130:133], v[180:187], v[220:227], v[130:133]
	v_mfma_f32_16x16x128_f8f6f4 v[122:125], v[188:195], v[220:227], v[122:125]
	v_mfma_f32_16x16x128_f8f6f4 v[114:117], v[180:187], v[228:235], v[114:117]
	v_mfma_f32_16x16x128_f8f6f4 v[106:109], v[188:195], v[228:235], v[106:109]
	v_mfma_f32_16x16x128_f8f6f4 v[98:101], v[180:187], v[236:243], v[98:101]
	v_mfma_f32_16x16x128_f8f6f4 v[90:93], v[188:195], v[236:243], v[90:93]
	v_mfma_f32_16x16x128_f8f6f4 v[82:85], v[180:187], v[244:251], v[82:85]
	v_mfma_f32_16x16x128_f8f6f4 v[66:69], v[188:195], v[244:251], v[66:69]
	s_setprio 0
	s_setprio 1
	v_mfma_f32_16x16x128_f8f6f4 v[134:137], v[204:211], v[220:227], v[134:137]
	v_mfma_f32_16x16x128_f8f6f4 v[126:129], v[212:219], v[220:227], v[126:129]
	v_mfma_f32_16x16x128_f8f6f4 v[118:121], v[204:211], v[228:235], v[118:121]
	v_mfma_f32_16x16x128_f8f6f4 v[110:113], v[212:219], v[228:235], v[110:113]
	v_mfma_f32_16x16x128_f8f6f4 v[102:105], v[204:211], v[236:243], v[102:105]
	v_mfma_f32_16x16x128_f8f6f4 v[94:97], v[212:219], v[236:243], v[94:97]
	v_mfma_f32_16x16x128_f8f6f4 v[86:89], v[204:211], v[244:251], v[86:89]
	v_mfma_f32_16x16x128_f8f6f4 v[74:77], v[212:219], v[244:251], v[74:77]
	s_setprio 0
	s_barrier
	s_mov_b32 m0, s86
	v_lshl_add_u64 v[160:161], v[156:157], 0, s[46:47]
	s_add_u32 s88, s78, 0x8200
	ds_read_b128 v[220:223], v166 offset:16384
	ds_read_b128 v[224:227], v166 offset:17408
	ds_read_b128 v[228:231], v166 offset:18432
	ds_read_b128 v[232:235], v166 offset:19456
	ds_read_b128 v[236:239], v166 offset:20480
	ds_read_b128 v[240:243], v166 offset:21504
	ds_read_b128 v[244:247], v166 offset:22528
	ds_read_b128 v[248:251], v166 offset:23552
	global_load_lds_dwordx4 v[160:161], off
	v_lshl_add_u64 v[160:161], v[158:159], 0, s[46:47]
	s_mov_b32 m0, s82
	s_addc_u32 s89, s79, 0
	global_load_lds_dwordx4 v[160:161], off
	v_lshl_add_u64 v[160:161], s[88:89], 0, v[138:139]
	s_mov_b32 m0, s83
	s_nop 0
	global_load_lds_dwordx4 v[160:161], off
	v_lshl_add_u64 v[160:161], s[88:89], 0, v[140:141]
	s_mov_b32 m0, s84
	s_nop 0
	global_load_lds_dwordx4 v[160:161], off
	s_mov_b32 m0, s55
	s_nop 0
	global_load_lds_dwordx4 v142, s[30:31]
	s_mov_b32 m0, s56
	s_nop 0
	global_load_lds_dwordx4 v154, s[30:31]
	s_waitcnt vmcnt(8)
	s_waitcnt lgkmcnt(0)
	s_barrier
	s_setprio 1
	s_waitcnt lgkmcnt(0)
	v_mfma_f32_16x16x128_f8f6f4 v[70:73], v[180:187], v[220:227], v[70:73]
	v_mfma_f32_16x16x128_f8f6f4 v[58:61], v[188:195], v[220:227], v[58:61]
	v_mfma_f32_16x16x128_f8f6f4 v[50:53], v[180:187], v[228:235], v[50:53]
	v_mfma_f32_16x16x128_f8f6f4 v[34:37], v[188:195], v[228:235], v[34:37]
	v_mfma_f32_16x16x128_f8f6f4 v[26:29], v[180:187], v[236:243], v[26:29]
	v_mfma_f32_16x16x128_f8f6f4 v[18:21], v[188:195], v[236:243], v[18:21]
	v_mfma_f32_16x16x128_f8f6f4 v[10:13], v[180:187], v[244:251], v[10:13]
	v_mfma_f32_16x16x128_f8f6f4 v[2:5], v[188:195], v[244:251], v[2:5]
	s_setprio 0
	s_setprio 1
	v_mfma_f32_16x16x128_f8f6f4 v[78:81], v[204:211], v[220:227], v[78:81]
	v_mfma_f32_16x16x128_f8f6f4 v[62:65], v[212:219], v[220:227], v[62:65]
	v_mfma_f32_16x16x128_f8f6f4 v[54:57], v[204:211], v[228:235], v[54:57]
	v_mfma_f32_16x16x128_f8f6f4 v[38:41], v[212:219], v[228:235], v[38:41]
	v_mfma_f32_16x16x128_f8f6f4 v[30:33], v[204:211], v[236:243], v[30:33]
	v_mfma_f32_16x16x128_f8f6f4 v[22:25], v[212:219], v[236:243], v[22:25]
	v_mfma_f32_16x16x128_f8f6f4 v[14:17], v[204:211], v[244:251], v[14:17]
	v_mfma_f32_16x16x128_f8f6f4 v[6:9], v[212:219], v[244:251], v[6:9]
	s_setprio 0
	s_barrier
	ds_read_b128 v[180:183], v147
	ds_read_b128 v[184:187], v147 offset:1024
	ds_read_b128 v[188:191], v147 offset:2048
	ds_read_b128 v[192:195], v147 offset:3072
	ds_read_b128 v[204:207], v149
	ds_read_b128 v[208:211], v149 offset:1024
	ds_read_b128 v[212:215], v149 offset:2048
	ds_read_b128 v[216:219], v149 offset:3072
	s_mov_b32 m0, s57
	ds_read_b128 v[220:223], v166 offset:32768
	ds_read_b128 v[224:227], v166 offset:33792
	ds_read_b128 v[228:231], v166 offset:34816
	ds_read_b128 v[232:235], v166 offset:35840
	ds_read_b128 v[236:239], v166 offset:36864
	ds_read_b128 v[240:243], v166 offset:37888
	ds_read_b128 v[244:247], v166 offset:38912
	ds_read_b128 v[248:251], v166 offset:39936
	global_load_lds_dwordx4 v152, s[30:31]
	s_mov_b32 m0, s58
	s_nop 0
	global_load_lds_dwordx4 v150, s[30:31]
	s_waitcnt vmcnt(8)
	s_waitcnt lgkmcnt(0)
	s_barrier
	s_setprio 1
	s_waitcnt lgkmcnt(0)
	v_mfma_f32_16x16x128_f8f6f4 v[130:133], v[180:187], v[220:227], v[130:133]
	v_mfma_f32_16x16x128_f8f6f4 v[122:125], v[188:195], v[220:227], v[122:125]
	v_mfma_f32_16x16x128_f8f6f4 v[114:117], v[180:187], v[228:235], v[114:117]
	v_mfma_f32_16x16x128_f8f6f4 v[106:109], v[188:195], v[228:235], v[106:109]
	v_mfma_f32_16x16x128_f8f6f4 v[98:101], v[180:187], v[236:243], v[98:101]
	v_mfma_f32_16x16x128_f8f6f4 v[90:93], v[188:195], v[236:243], v[90:93]
	v_mfma_f32_16x16x128_f8f6f4 v[82:85], v[180:187], v[244:251], v[82:85]
	v_mfma_f32_16x16x128_f8f6f4 v[66:69], v[188:195], v[244:251], v[66:69]
	s_setprio 0
	s_setprio 1
	v_mfma_f32_16x16x128_f8f6f4 v[134:137], v[204:211], v[220:227], v[134:137]
	v_mfma_f32_16x16x128_f8f6f4 v[126:129], v[212:219], v[220:227], v[126:129]
	v_mfma_f32_16x16x128_f8f6f4 v[118:121], v[204:211], v[228:235], v[118:121]
	v_mfma_f32_16x16x128_f8f6f4 v[110:113], v[212:219], v[228:235], v[110:113]
	v_mfma_f32_16x16x128_f8f6f4 v[102:105], v[204:211], v[236:243], v[102:105]
	v_mfma_f32_16x16x128_f8f6f4 v[94:97], v[212:219], v[236:243], v[94:97]
	v_mfma_f32_16x16x128_f8f6f4 v[86:89], v[204:211], v[244:251], v[86:89]
	v_mfma_f32_16x16x128_f8f6f4 v[74:77], v[212:219], v[244:251], v[74:77]
	s_setprio 0
	s_barrier
	s_mov_b32 m0, s85
	v_lshl_add_u64 v[160:161], v[156:157], 0, s[48:49]
	s_add_u32 s88, s78, 0x8280
	ds_read_b128 v[220:223], v166 offset:49152
	ds_read_b128 v[224:227], v166 offset:50176
	ds_read_b128 v[228:231], v166 offset:51200
	ds_read_b128 v[232:235], v166 offset:52224
	ds_read_b128 v[236:239], v166 offset:53248
	ds_read_b128 v[240:243], v166 offset:54272
	ds_read_b128 v[244:247], v166 offset:55296
	ds_read_b128 v[248:251], v166 offset:56320
	global_load_lds_dwordx4 v[160:161], off
	v_lshl_add_u64 v[160:161], v[158:159], 0, s[48:49]
	s_mov_b32 m0, s65
	s_addc_u32 s89, s79, 0
	global_load_lds_dwordx4 v[160:161], off
	v_lshl_add_u64 v[160:161], s[88:89], 0, v[138:139]
	s_mov_b32 m0, s67
	s_nop 0
	global_load_lds_dwordx4 v[160:161], off
	v_lshl_add_u64 v[160:161], s[88:89], 0, v[140:141]
	s_mov_b32 m0, s68
	s_nop 0
	global_load_lds_dwordx4 v[160:161], off
	s_mov_b32 m0, s59
	s_nop 0
	global_load_lds_dwordx4 v142, s[34:35]
	s_mov_b32 m0, s60
	s_nop 0
	global_load_lds_dwordx4 v154, s[34:35]
	s_waitcnt vmcnt(8)
	s_waitcnt lgkmcnt(0)
	s_barrier
	s_setprio 1
	s_waitcnt lgkmcnt(0)
	v_mfma_f32_16x16x128_f8f6f4 v[70:73], v[180:187], v[220:227], v[70:73]
	v_mfma_f32_16x16x128_f8f6f4 v[58:61], v[188:195], v[220:227], v[58:61]
	v_mfma_f32_16x16x128_f8f6f4 v[50:53], v[180:187], v[228:235], v[50:53]
	v_mfma_f32_16x16x128_f8f6f4 v[34:37], v[188:195], v[228:235], v[34:37]
	v_mfma_f32_16x16x128_f8f6f4 v[26:29], v[180:187], v[236:243], v[26:29]
	v_mfma_f32_16x16x128_f8f6f4 v[18:21], v[188:195], v[236:243], v[18:21]
	v_mfma_f32_16x16x128_f8f6f4 v[10:13], v[180:187], v[244:251], v[10:13]
	v_mfma_f32_16x16x128_f8f6f4 v[2:5], v[188:195], v[244:251], v[2:5]
	s_setprio 0
	s_setprio 1
	v_mfma_f32_16x16x128_f8f6f4 v[78:81], v[204:211], v[220:227], v[78:81]
	v_mfma_f32_16x16x128_f8f6f4 v[62:65], v[212:219], v[220:227], v[62:65]
	v_mfma_f32_16x16x128_f8f6f4 v[54:57], v[204:211], v[228:235], v[54:57]
	v_mfma_f32_16x16x128_f8f6f4 v[38:41], v[212:219], v[228:235], v[38:41]
	v_mfma_f32_16x16x128_f8f6f4 v[30:33], v[204:211], v[236:243], v[30:33]
	v_mfma_f32_16x16x128_f8f6f4 v[22:25], v[212:219], v[236:243], v[22:25]
	v_mfma_f32_16x16x128_f8f6f4 v[14:17], v[204:211], v[244:251], v[14:17]
	v_mfma_f32_16x16x128_f8f6f4 v[6:9], v[212:219], v[244:251], v[6:9]
	s_setprio 0
	s_barrier
	ds_read_b128 v[180:183], v167
	ds_read_b128 v[184:187], v167 offset:1024
	ds_read_b128 v[188:191], v167 offset:2048
	ds_read_b128 v[192:195], v167 offset:3072
	ds_read_b128 v[204:207], v168
	ds_read_b128 v[208:211], v168 offset:1024
	ds_read_b128 v[212:215], v168 offset:2048
	ds_read_b128 v[216:219], v168 offset:3072
	s_mov_b32 m0, s61
	ds_read_b128 v[220:223], v166
	ds_read_b128 v[224:227], v166 offset:1024
	ds_read_b128 v[228:231], v166 offset:2048
	ds_read_b128 v[232:235], v166 offset:3072
	ds_read_b128 v[236:239], v166 offset:4096
	ds_read_b128 v[240:243], v166 offset:5120
	ds_read_b128 v[244:247], v166 offset:6144
	ds_read_b128 v[248:251], v166 offset:7168
	global_load_lds_dwordx4 v152, s[34:35]
	s_mov_b32 m0, s69
	s_nop 0
	global_load_lds_dwordx4 v150, s[34:35]
	s_waitcnt vmcnt(8)
	s_waitcnt lgkmcnt(0)
	s_barrier
	s_setprio 1
	s_waitcnt lgkmcnt(0)
	v_mfma_f32_16x16x128_f8f6f4 v[130:133], v[180:187], v[220:227], v[130:133]
	v_mfma_f32_16x16x128_f8f6f4 v[122:125], v[188:195], v[220:227], v[122:125]
	v_mfma_f32_16x16x128_f8f6f4 v[114:117], v[180:187], v[228:235], v[114:117]
	v_mfma_f32_16x16x128_f8f6f4 v[106:109], v[188:195], v[228:235], v[106:109]
	v_mfma_f32_16x16x128_f8f6f4 v[98:101], v[180:187], v[236:243], v[98:101]
	v_mfma_f32_16x16x128_f8f6f4 v[90:93], v[188:195], v[236:243], v[90:93]
	v_mfma_f32_16x16x128_f8f6f4 v[82:85], v[180:187], v[244:251], v[82:85]
	v_mfma_f32_16x16x128_f8f6f4 v[66:69], v[188:195], v[244:251], v[66:69]
	s_setprio 0
	s_setprio 1
	v_mfma_f32_16x16x128_f8f6f4 v[134:137], v[204:211], v[220:227], v[134:137]
	v_mfma_f32_16x16x128_f8f6f4 v[126:129], v[212:219], v[220:227], v[126:129]
	v_mfma_f32_16x16x128_f8f6f4 v[118:121], v[204:211], v[228:235], v[118:121]
	v_mfma_f32_16x16x128_f8f6f4 v[110:113], v[212:219], v[228:235], v[110:113]
	v_mfma_f32_16x16x128_f8f6f4 v[102:105], v[204:211], v[236:243], v[102:105]
	v_mfma_f32_16x16x128_f8f6f4 v[94:97], v[212:219], v[236:243], v[94:97]
	v_mfma_f32_16x16x128_f8f6f4 v[86:89], v[204:211], v[244:251], v[86:89]
	v_mfma_f32_16x16x128_f8f6f4 v[74:77], v[212:219], v[244:251], v[74:77]
	s_setprio 0
	s_barrier
	s_mov_b32 m0, s86
	v_lshl_add_u64 v[160:161], v[156:157], 0, s[50:51]
	s_add_u32 s88, s78, 0x8300
	ds_read_b128 v[220:223], v166 offset:16384
	ds_read_b128 v[224:227], v166 offset:17408
	ds_read_b128 v[228:231], v166 offset:18432
	ds_read_b128 v[232:235], v166 offset:19456
	ds_read_b128 v[236:239], v166 offset:20480
	ds_read_b128 v[240:243], v166 offset:21504
	ds_read_b128 v[244:247], v166 offset:22528
	ds_read_b128 v[248:251], v166 offset:23552
	global_load_lds_dwordx4 v[160:161], off
	v_lshl_add_u64 v[160:161], v[158:159], 0, s[50:51]
	s_mov_b32 m0, s82
	s_addc_u32 s89, s79, 0
	global_load_lds_dwordx4 v[160:161], off
	v_lshl_add_u64 v[160:161], s[88:89], 0, v[138:139]
	s_mov_b32 m0, s83
	s_nop 0
	global_load_lds_dwordx4 v[160:161], off
	v_lshl_add_u64 v[160:161], s[88:89], 0, v[140:141]
	s_mov_b32 m0, s84
	s_nop 0
	global_load_lds_dwordx4 v[160:161], off
	s_mov_b32 m0, s55
	s_nop 0
	global_load_lds_dwordx4 v142, s[36:37]
	s_mov_b32 m0, s56
	s_nop 0
	global_load_lds_dwordx4 v154, s[36:37]
	s_waitcnt vmcnt(8)
	s_waitcnt lgkmcnt(0)
	s_barrier
	s_setprio 1
	s_waitcnt lgkmcnt(0)
	v_mfma_f32_16x16x128_f8f6f4 v[70:73], v[180:187], v[220:227], v[70:73]
	v_mfma_f32_16x16x128_f8f6f4 v[58:61], v[188:195], v[220:227], v[58:61]
	v_mfma_f32_16x16x128_f8f6f4 v[50:53], v[180:187], v[228:235], v[50:53]
	v_mfma_f32_16x16x128_f8f6f4 v[34:37], v[188:195], v[228:235], v[34:37]
	v_mfma_f32_16x16x128_f8f6f4 v[26:29], v[180:187], v[236:243], v[26:29]
	v_mfma_f32_16x16x128_f8f6f4 v[18:21], v[188:195], v[236:243], v[18:21]
	v_mfma_f32_16x16x128_f8f6f4 v[10:13], v[180:187], v[244:251], v[10:13]
	v_mfma_f32_16x16x128_f8f6f4 v[2:5], v[188:195], v[244:251], v[2:5]
	s_setprio 0
	s_setprio 1
	v_mfma_f32_16x16x128_f8f6f4 v[78:81], v[204:211], v[220:227], v[78:81]
	v_mfma_f32_16x16x128_f8f6f4 v[62:65], v[212:219], v[220:227], v[62:65]
	v_mfma_f32_16x16x128_f8f6f4 v[54:57], v[204:211], v[228:235], v[54:57]
	v_mfma_f32_16x16x128_f8f6f4 v[38:41], v[212:219], v[228:235], v[38:41]
	v_mfma_f32_16x16x128_f8f6f4 v[30:33], v[204:211], v[236:243], v[30:33]
	v_mfma_f32_16x16x128_f8f6f4 v[22:25], v[212:219], v[236:243], v[22:25]
	v_mfma_f32_16x16x128_f8f6f4 v[14:17], v[204:211], v[244:251], v[14:17]
	v_mfma_f32_16x16x128_f8f6f4 v[6:9], v[212:219], v[244:251], v[6:9]
	s_setprio 0
	s_barrier
	ds_read_b128 v[180:183], v147
	ds_read_b128 v[184:187], v147 offset:1024
	ds_read_b128 v[188:191], v147 offset:2048
	ds_read_b128 v[192:195], v147 offset:3072
	ds_read_b128 v[204:207], v149
	ds_read_b128 v[208:211], v149 offset:1024
	ds_read_b128 v[212:215], v149 offset:2048
	ds_read_b128 v[216:219], v149 offset:3072
	s_mov_b32 m0, s57
	ds_read_b128 v[220:223], v166 offset:32768
	ds_read_b128 v[224:227], v166 offset:33792
	ds_read_b128 v[228:231], v166 offset:34816
	ds_read_b128 v[232:235], v166 offset:35840
	ds_read_b128 v[236:239], v166 offset:36864
	ds_read_b128 v[240:243], v166 offset:37888
	ds_read_b128 v[244:247], v166 offset:38912
	ds_read_b128 v[248:251], v166 offset:39936
	global_load_lds_dwordx4 v152, s[36:37]
	s_mov_b32 m0, s58
	s_nop 0
	global_load_lds_dwordx4 v150, s[36:37]
	s_waitcnt vmcnt(8)
	s_waitcnt lgkmcnt(0)
	s_barrier
	s_setprio 1
	s_waitcnt lgkmcnt(0)
	v_mfma_f32_16x16x128_f8f6f4 v[130:133], v[180:187], v[220:227], v[130:133]
	v_mfma_f32_16x16x128_f8f6f4 v[122:125], v[188:195], v[220:227], v[122:125]
	v_mfma_f32_16x16x128_f8f6f4 v[114:117], v[180:187], v[228:235], v[114:117]
	v_mfma_f32_16x16x128_f8f6f4 v[106:109], v[188:195], v[228:235], v[106:109]
	v_mfma_f32_16x16x128_f8f6f4 v[98:101], v[180:187], v[236:243], v[98:101]
	v_mfma_f32_16x16x128_f8f6f4 v[90:93], v[188:195], v[236:243], v[90:93]
	v_mfma_f32_16x16x128_f8f6f4 v[82:85], v[180:187], v[244:251], v[82:85]
	v_mfma_f32_16x16x128_f8f6f4 v[66:69], v[188:195], v[244:251], v[66:69]
	s_setprio 0
	s_setprio 1
	v_mfma_f32_16x16x128_f8f6f4 v[134:137], v[204:211], v[220:227], v[134:137]
	v_mfma_f32_16x16x128_f8f6f4 v[126:129], v[212:219], v[220:227], v[126:129]
	v_mfma_f32_16x16x128_f8f6f4 v[118:121], v[204:211], v[228:235], v[118:121]
	v_mfma_f32_16x16x128_f8f6f4 v[110:113], v[212:219], v[228:235], v[110:113]
	v_mfma_f32_16x16x128_f8f6f4 v[102:105], v[204:211], v[236:243], v[102:105]
	v_mfma_f32_16x16x128_f8f6f4 v[94:97], v[212:219], v[236:243], v[94:97]
	v_mfma_f32_16x16x128_f8f6f4 v[86:89], v[204:211], v[244:251], v[86:89]
	v_mfma_f32_16x16x128_f8f6f4 v[74:77], v[212:219], v[244:251], v[74:77]
	s_setprio 0
	s_barrier
	s_mov_b32 m0, s85
	v_lshl_add_u64 v[156:157], v[156:157], 0, s[62:63]
	s_add_u32 s78, s78, 0x8380
	ds_read_b128 v[220:223], v166 offset:49152
	ds_read_b128 v[224:227], v166 offset:50176
	ds_read_b128 v[228:231], v166 offset:51200
	ds_read_b128 v[232:235], v166 offset:52224
	ds_read_b128 v[236:239], v166 offset:53248
	ds_read_b128 v[240:243], v166 offset:54272
	ds_read_b128 v[244:247], v166 offset:55296
	ds_read_b128 v[248:251], v166 offset:56320
	global_load_lds_dwordx4 v[156:157], off
	v_lshl_add_u64 v[156:157], v[158:159], 0, s[62:63]
	s_mov_b32 m0, s65
	s_addc_u32 s79, s79, 0
	global_load_lds_dwordx4 v[156:157], off
	v_lshl_add_u64 v[156:157], s[78:79], 0, v[138:139]
	s_mov_b32 m0, s67
	s_nop 0
	global_load_lds_dwordx4 v[156:157], off
	v_lshl_add_u64 v[156:157], s[78:79], 0, v[140:141]
	s_mov_b32 m0, s68
	s_nop 0
	global_load_lds_dwordx4 v[156:157], off
	s_mov_b32 m0, s59
	s_nop 0
	global_load_lds_dwordx4 v142, s[38:39]
	s_mov_b32 m0, s60
	s_nop 0
	global_load_lds_dwordx4 v154, s[38:39]
	s_waitcnt vmcnt(8)
	s_waitcnt lgkmcnt(0)
	s_barrier
	s_setprio 1
	s_waitcnt lgkmcnt(0)
	v_mfma_f32_16x16x128_f8f6f4 v[70:73], v[180:187], v[220:227], v[70:73]
	v_mfma_f32_16x16x128_f8f6f4 v[58:61], v[188:195], v[220:227], v[58:61]
	v_mfma_f32_16x16x128_f8f6f4 v[50:53], v[180:187], v[228:235], v[50:53]
	v_mfma_f32_16x16x128_f8f6f4 v[34:37], v[188:195], v[228:235], v[34:37]
	v_mfma_f32_16x16x128_f8f6f4 v[26:29], v[180:187], v[236:243], v[26:29]
	v_mfma_f32_16x16x128_f8f6f4 v[18:21], v[188:195], v[236:243], v[18:21]
	v_mfma_f32_16x16x128_f8f6f4 v[10:13], v[180:187], v[244:251], v[10:13]
	v_mfma_f32_16x16x128_f8f6f4 v[2:5], v[188:195], v[244:251], v[2:5]
	s_setprio 0
	s_setprio 1
	v_mfma_f32_16x16x128_f8f6f4 v[78:81], v[204:211], v[220:227], v[78:81]
	v_mfma_f32_16x16x128_f8f6f4 v[62:65], v[212:219], v[220:227], v[62:65]
	v_mfma_f32_16x16x128_f8f6f4 v[54:57], v[204:211], v[228:235], v[54:57]
	v_mfma_f32_16x16x128_f8f6f4 v[38:41], v[212:219], v[228:235], v[38:41]
	v_mfma_f32_16x16x128_f8f6f4 v[30:33], v[204:211], v[236:243], v[30:33]
	v_mfma_f32_16x16x128_f8f6f4 v[22:25], v[212:219], v[236:243], v[22:25]
	v_mfma_f32_16x16x128_f8f6f4 v[14:17], v[204:211], v[244:251], v[14:17]
	v_mfma_f32_16x16x128_f8f6f4 v[6:9], v[212:219], v[244:251], v[6:9]
	s_setprio 0
	s_barrier
	ds_read_b128 v[154:157], v167
	ds_read_b128 v[158:161], v167 offset:1024
	ds_read_b128 v[180:183], v167 offset:2048
	ds_read_b128 v[184:187], v167 offset:3072
	ds_read_b128 v[188:191], v168
	ds_read_b128 v[192:195], v168 offset:1024
	ds_read_b128 v[204:207], v168 offset:2048
	ds_read_b128 v[208:211], v168 offset:3072
	s_mov_b32 m0, s61
	ds_read_b128 v[212:215], v166
	ds_read_b128 v[216:219], v166 offset:1024
	ds_read_b128 v[220:223], v166 offset:2048
	ds_read_b128 v[224:227], v166 offset:3072
	ds_read_b128 v[228:231], v166 offset:4096
	ds_read_b128 v[232:235], v166 offset:5120
	ds_read_b128 v[236:239], v166 offset:6144
	ds_read_b128 v[240:243], v166 offset:7168
	global_load_lds_dwordx4 v152, s[38:39]
	s_mov_b32 m0, s69
	s_nop 0
	global_load_lds_dwordx4 v150, s[38:39]
	s_waitcnt vmcnt(8)
	s_waitcnt lgkmcnt(0)
	s_barrier
	s_setprio 1
	s_waitcnt lgkmcnt(0)
	v_mfma_f32_16x16x128_f8f6f4 v[130:133], v[154:161], v[212:219], v[130:133]
	v_mfma_f32_16x16x128_f8f6f4 v[122:125], v[180:187], v[212:219], v[122:125]
	v_mfma_f32_16x16x128_f8f6f4 v[114:117], v[154:161], v[220:227], v[114:117]
	v_mfma_f32_16x16x128_f8f6f4 v[106:109], v[180:187], v[220:227], v[106:109]
	v_mfma_f32_16x16x128_f8f6f4 v[98:101], v[154:161], v[228:235], v[98:101]
	v_mfma_f32_16x16x128_f8f6f4 v[90:93], v[180:187], v[228:235], v[90:93]
	v_mfma_f32_16x16x128_f8f6f4 v[82:85], v[154:161], v[236:243], v[82:85]
	v_mfma_f32_16x16x128_f8f6f4 v[66:69], v[180:187], v[236:243], v[66:69]
	s_setprio 0
	s_setprio 1
	v_mfma_f32_16x16x128_f8f6f4 v[134:137], v[188:195], v[212:219], v[134:137]
	v_mfma_f32_16x16x128_f8f6f4 v[126:129], v[204:211], v[212:219], v[126:129]
	v_mfma_f32_16x16x128_f8f6f4 v[118:121], v[188:195], v[220:227], v[118:121]
	v_mfma_f32_16x16x128_f8f6f4 v[110:113], v[204:211], v[220:227], v[110:113]
	v_mfma_f32_16x16x128_f8f6f4 v[102:105], v[188:195], v[228:235], v[102:105]
	v_mfma_f32_16x16x128_f8f6f4 v[94:97], v[204:211], v[228:235], v[94:97]
	v_mfma_f32_16x16x128_f8f6f4 v[86:89], v[188:195], v[236:243], v[86:89]
	v_mfma_f32_16x16x128_f8f6f4 v[74:77], v[204:211], v[236:243], v[74:77]
	s_setprio 0
	s_barrier
	s_cmp_lg_u64 s[8:9], 0
	s_cbranch_scc1 .Lgu1_rm_skip
	v_lshlrev_b32_e32 v200, 10, v200
	v_lshlrev_b32_e32 v201, 10, v201
	v_lshlrev_b32_e32 v252, 10, v252
	v_lshlrev_b32_e32 v253, 10, v253
	v_and_b32_e32 v200, 0x3fffc00, v200
	v_and_b32_e32 v201, 0x3fffc00, v201
	v_and_b32_e32 v253, 0x3fffc00, v253
	v_and_b32_e32 v252, 0x3fffc00, v252
	v_add_u32_e32 v172, v200, v163
	v_add_u32_e32 v173, v201, v164
	v_add_u32_e32 v146, v253, v163
	v_add_u32_e32 v148, v252, v164
.Lgu1_rm_skip:
	s_mov_b32 m0, s86
	v_lshl_add_u64 v[196:197], s[10:11], 0, v[138:139]
	s_add_u32 s78, s10, 0x8000
	ds_read_b128 v[212:215], v166 offset:16384
	ds_read_b128 v[216:219], v166 offset:17408
	ds_read_b128 v[220:223], v166 offset:18432
	ds_read_b128 v[224:227], v166 offset:19456
	ds_read_b128 v[228:231], v166 offset:20480
	ds_read_b128 v[232:235], v166 offset:21504
	ds_read_b128 v[236:239], v166 offset:22528
	ds_read_b128 v[240:243], v166 offset:23552
	global_load_lds_dwordx4 v[196:197], off
	v_lshl_add_u64 v[198:199], s[10:11], 0, v[140:141]
	s_mov_b32 m0, s82
	s_addc_u32 s79, s11, 0
	global_load_lds_dwordx4 v[198:199], off
	v_lshl_add_u64 v[150:151], s[78:79], 0, v[138:139]
	s_mov_b32 m0, s83
	s_nop 0
	global_load_lds_dwordx4 v[150:151], off
	v_lshl_add_u64 v[150:151], s[78:79], 0, v[140:141]
	s_mov_b32 m0, s84
	s_nop 0
	global_load_lds_dwordx4 v[150:151], off
	s_mov_b32 m0, s55
	s_nop 0
	global_load_lds_dwordx4 v172, s[12:13]
	s_mov_b32 m0, s56
	s_nop 0
	global_load_lds_dwordx4 v173, s[12:13]
	s_waitcnt vmcnt(8)
	s_waitcnt lgkmcnt(0)
	s_barrier
	s_setprio 1
	s_waitcnt lgkmcnt(0)
	v_mfma_f32_16x16x128_f8f6f4 v[70:73], v[154:161], v[212:219], v[70:73]
	v_mfma_f32_16x16x128_f8f6f4 v[58:61], v[180:187], v[212:219], v[58:61]
	v_mfma_f32_16x16x128_f8f6f4 v[50:53], v[154:161], v[220:227], v[50:53]
	v_mfma_f32_16x16x128_f8f6f4 v[34:37], v[180:187], v[220:227], v[34:37]
	v_mfma_f32_16x16x128_f8f6f4 v[26:29], v[154:161], v[228:235], v[26:29]
	v_mfma_f32_16x16x128_f8f6f4 v[18:21], v[180:187], v[228:235], v[18:21]
	v_mfma_f32_16x16x128_f8f6f4 v[10:13], v[154:161], v[236:243], v[10:13]
	v_mfma_f32_16x16x128_f8f6f4 v[2:5], v[180:187], v[236:243], v[2:5]
	s_setprio 0
	s_setprio 1
	v_mfma_f32_16x16x128_f8f6f4 v[78:81], v[188:195], v[212:219], v[78:81]
	v_mfma_f32_16x16x128_f8f6f4 v[62:65], v[204:211], v[212:219], v[62:65]
	v_mfma_f32_16x16x128_f8f6f4 v[54:57], v[188:195], v[220:227], v[54:57]
	v_mfma_f32_16x16x128_f8f6f4 v[38:41], v[204:211], v[220:227], v[38:41]
	v_mfma_f32_16x16x128_f8f6f4 v[30:33], v[188:195], v[228:235], v[30:33]
	v_mfma_f32_16x16x128_f8f6f4 v[22:25], v[204:211], v[228:235], v[22:25]
	v_mfma_f32_16x16x128_f8f6f4 v[14:17], v[188:195], v[236:243], v[14:17]
	v_mfma_f32_16x16x128_f8f6f4 v[6:9], v[204:211], v[236:243], v[6:9]
	s_setprio 0
	s_barrier
	ds_read_b128 v[150:153], v147
	ds_read_b128 v[154:157], v147 offset:1024
	ds_read_b128 v[180:183], v147 offset:2048
	ds_read_b128 v[184:187], v147 offset:3072
	ds_read_b128 v[188:191], v149
	ds_read_b128 v[192:195], v149 offset:1024
	ds_read_b128 v[204:207], v149 offset:2048
	ds_read_b128 v[208:211], v149 offset:3072
	s_mov_b32 m0, s57
	ds_read_b128 v[212:215], v166 offset:32768
	ds_read_b128 v[216:219], v166 offset:33792
	ds_read_b128 v[220:223], v166 offset:34816
	ds_read_b128 v[224:227], v166 offset:35840
	ds_read_b128 v[228:231], v166 offset:36864
	ds_read_b128 v[232:235], v166 offset:37888
	ds_read_b128 v[236:239], v166 offset:38912
	ds_read_b128 v[240:243], v166 offset:39936
	global_load_lds_dwordx4 v146, s[12:13]
	s_mov_b32 m0, s58
	s_nop 0
	global_load_lds_dwordx4 v148, s[12:13]
	s_waitcnt vmcnt(8)
	s_waitcnt lgkmcnt(0)
	s_barrier
	s_setprio 1
	s_waitcnt lgkmcnt(0)
	v_mfma_f32_16x16x128_f8f6f4 v[130:133], v[150:157], v[212:219], v[130:133]
	v_mfma_f32_16x16x128_f8f6f4 v[122:125], v[180:187], v[212:219], v[122:125]
	v_mfma_f32_16x16x128_f8f6f4 v[114:117], v[150:157], v[220:227], v[114:117]
	v_mfma_f32_16x16x128_f8f6f4 v[106:109], v[180:187], v[220:227], v[106:109]
	v_mfma_f32_16x16x128_f8f6f4 v[98:101], v[150:157], v[228:235], v[98:101]
	v_mfma_f32_16x16x128_f8f6f4 v[90:93], v[180:187], v[228:235], v[90:93]
	v_mfma_f32_16x16x128_f8f6f4 v[82:85], v[150:157], v[236:243], v[82:85]
	v_mfma_f32_16x16x128_f8f6f4 v[66:69], v[180:187], v[236:243], v[66:69]
	s_setprio 0
	s_setprio 1
	v_mfma_f32_16x16x128_f8f6f4 v[134:137], v[188:195], v[212:219], v[134:137]
	v_mfma_f32_16x16x128_f8f6f4 v[126:129], v[204:211], v[212:219], v[126:129]
	v_mfma_f32_16x16x128_f8f6f4 v[118:121], v[188:195], v[220:227], v[118:121]
	v_mfma_f32_16x16x128_f8f6f4 v[110:113], v[204:211], v[220:227], v[110:113]
	v_mfma_f32_16x16x128_f8f6f4 v[102:105], v[188:195], v[228:235], v[102:105]
	v_mfma_f32_16x16x128_f8f6f4 v[94:97], v[204:211], v[228:235], v[94:97]
	v_mfma_f32_16x16x128_f8f6f4 v[86:89], v[188:195], v[236:243], v[86:89]
	v_mfma_f32_16x16x128_f8f6f4 v[74:77], v[204:211], v[236:243], v[74:77]
	s_setprio 0
	s_barrier
	s_mov_b32 m0, s85
	v_lshl_add_u64 v[158:159], v[196:197], 0, s[20:21]
	s_add_u32 s10, s10, 0x8080
	ds_read_b128 v[212:215], v166 offset:49152
	ds_read_b128 v[216:219], v166 offset:50176
	ds_read_b128 v[220:223], v166 offset:51200
	ds_read_b128 v[224:227], v166 offset:52224
	ds_read_b128 v[228:231], v166 offset:53248
	ds_read_b128 v[232:235], v166 offset:54272
	ds_read_b128 v[236:239], v166 offset:55296
	ds_read_b128 v[240:243], v166 offset:56320
	global_load_lds_dwordx4 v[158:159], off
	v_lshl_add_u64 v[158:159], v[198:199], 0, s[20:21]
	s_mov_b32 m0, s65
	s_addc_u32 s11, s11, 0
	global_load_lds_dwordx4 v[158:159], off
	v_lshl_add_u64 v[158:159], s[10:11], 0, v[138:139]
	s_mov_b32 m0, s67
	s_nop 0
	global_load_lds_dwordx4 v[158:159], off
	v_lshl_add_u64 v[158:159], s[10:11], 0, v[140:141]
	s_mov_b32 m0, s68
	s_nop 0
	global_load_lds_dwordx4 v[158:159], off
	s_mov_b32 m0, s59
	s_nop 0
	global_load_lds_dwordx4 v172, s[22:23]
	s_mov_b32 m0, s60
	s_nop 0
	global_load_lds_dwordx4 v173, s[22:23]
	s_waitcnt vmcnt(8)
	s_waitcnt lgkmcnt(0)
	s_barrier
	s_setprio 1
	s_waitcnt lgkmcnt(0)
	v_mfma_f32_16x16x128_f8f6f4 v[70:73], v[150:157], v[212:219], v[70:73]
	v_mfma_f32_16x16x128_f8f6f4 v[58:61], v[180:187], v[212:219], v[58:61]
	v_mfma_f32_16x16x128_f8f6f4 v[50:53], v[150:157], v[220:227], v[50:53]
	v_mfma_f32_16x16x128_f8f6f4 v[34:37], v[180:187], v[220:227], v[34:37]
	v_mfma_f32_16x16x128_f8f6f4 v[26:29], v[150:157], v[228:235], v[26:29]
	v_mfma_f32_16x16x128_f8f6f4 v[18:21], v[180:187], v[228:235], v[18:21]
	v_mfma_f32_16x16x128_f8f6f4 v[10:13], v[150:157], v[236:243], v[10:13]
	v_mfma_f32_16x16x128_f8f6f4 v[2:5], v[180:187], v[236:243], v[2:5]
	s_setprio 0
	s_setprio 1
	v_mfma_f32_16x16x128_f8f6f4 v[78:81], v[188:195], v[212:219], v[78:81]
	v_mfma_f32_16x16x128_f8f6f4 v[62:65], v[204:211], v[212:219], v[62:65]
	v_mfma_f32_16x16x128_f8f6f4 v[54:57], v[188:195], v[220:227], v[54:57]
	v_mfma_f32_16x16x128_f8f6f4 v[38:41], v[204:211], v[220:227], v[38:41]
	v_mfma_f32_16x16x128_f8f6f4 v[30:33], v[188:195], v[228:235], v[30:33]
	v_mfma_f32_16x16x128_f8f6f4 v[22:25], v[204:211], v[228:235], v[22:25]
	v_mfma_f32_16x16x128_f8f6f4 v[14:17], v[188:195], v[236:243], v[14:17]
	v_mfma_f32_16x16x128_f8f6f4 v[6:9], v[204:211], v[236:243], v[6:9]
	s_setprio 0
	s_barrier
	s_and_b64 vcc, exec, s[8:9]
	s_cbranch_vccnz .LBB0_3346
	v_mov_b32_e32 v147, v143
	s_mov_b32 m0, s61
	v_mov_b32_e32 v149, v143
	v_lshl_add_u64 v[150:151], s[22:23], 0, v[146:147]
	v_lshl_add_u64 v[152:153], s[22:23], 0, v[148:149]
	global_load_lds_dwordx4 v[150:151], off
	s_mov_b32 m0, s69
	s_nop 0
	global_load_lds_dwordx4 v[152:153], off
